# v19
# baseline (speedup 1.0000x reference)
.LBB0_40:
	s_load_dword s6, s[22:23], 0x0
	s_lshl_b32 s12, s30, 2
	s_add_u32 s8, s16, s12
	s_addc_u32 s9, s17, 0
	s_waitcnt vmcnt(13)
	v_lshlrev_b32_e32 v42, 4, v209
	s_add_u32 s12, s18, s12
	s_addc_u32 s13, s19, 0
	global_load_dwordx4 v[38:41], v42, s[8:9]
	global_load_dwordx4 v[34:37], v42, s[12:13]
	s_lshl_b32 s36, s27, 3
	s_add_i32 s36, s36, s31
	s_mul_i32 s37, s36, 0x210
	s_add_i32 s37, s37, 0x23440
	s_mov_b32 s14, 0xaaaaaaaa
	s_mov_b32 s15, 0xaaaaaaaa
	s_mov_b32 s24, 0xcccccccc
	s_mov_b32 s25, 0xcccccccc
	v_mov_b32_e32 v42, v218
	s_nop 1
	v_max_f32_dpp v42, v42, v42 quad_perm:[1,0,3,2] row_mask:0xf bank_mask:0xf
	s_nop 1
	v_max_f32_dpp v42, v42, v42 quad_perm:[2,3,0,1] row_mask:0xf bank_mask:0xf
	s_nop 1
	v_max_f32_dpp v42, v42, v42 row_half_mirror row_mask:0xf bank_mask:0xf
	s_nop 1
	v_max_f32_dpp v42, v42, v42 row_mirror row_mask:0xf bank_mask:0xf
	v_sub_f32_e32 v44, v218, v42
	v_exp_f32_e32 v44, v44
	v_and_b32_e32 v47, 3, v131
	v_lshl_add_u32 v47, v47, 2, v203
	v_mul_f32_e32 v43, v219, v44
	v_pk_mul_f32 v[48:49], v[198:199], v[44:45] op_sel_hi:[1,0]
	v_pk_mul_f32 v[50:51], v[196:197], v[44:45] op_sel_hi:[1,0]
	v_pk_mul_f32 v[52:53], v[194:195], v[44:45] op_sel_hi:[1,0]
	v_pk_mul_f32 v[54:55], v[192:193], v[44:45] op_sel_hi:[1,0]
	v_pk_mul_f32 v[56:57], v[190:191], v[44:45] op_sel_hi:[1,0]
	v_pk_mul_f32 v[58:59], v[188:189], v[44:45] op_sel_hi:[1,0]
	v_pk_mul_f32 v[60:61], v[186:187], v[44:45] op_sel_hi:[1,0]
	v_pk_mul_f32 v[62:63], v[184:185], v[44:45] op_sel_hi:[1,0]
	v_pk_mul_f32 v[64:65], v[182:183], v[44:45] op_sel_hi:[1,0]
	v_pk_mul_f32 v[66:67], v[180:181], v[44:45] op_sel_hi:[1,0]
	v_pk_mul_f32 v[68:69], v[178:179], v[44:45] op_sel_hi:[1,0]
	v_pk_mul_f32 v[70:71], v[168:169], v[44:45] op_sel_hi:[1,0]
	v_pk_mul_f32 v[72:73], v[150:151], v[44:45] op_sel_hi:[1,0]
	v_pk_mul_f32 v[74:75], v[140:141], v[44:45] op_sel_hi:[1,0]
	v_pk_mul_f32 v[76:77], v[138:139], v[44:45] op_sel_hi:[1,0]
	v_pk_mul_f32 v[78:79], v[136:137], v[44:45] op_sel_hi:[1,0]
	v_add_u32_e32 v47, s37, v47
	v_add_f32_dpp v43, v43, v43 row_shr:1 row_mask:0xf bank_mask:0xf
	v_cndmask_b32_e64 v80, v48, v49, s[14:15]
	v_cndmask_b32_e64 v49, v49, v48, s[14:15]
	v_cndmask_b32_e64 v81, v50, v51, s[14:15]
	v_cndmask_b32_e64 v51, v51, v50, s[14:15]
	v_cndmask_b32_e64 v82, v52, v53, s[14:15]
	v_cndmask_b32_e64 v53, v53, v52, s[14:15]
	v_cndmask_b32_e64 v83, v54, v55, s[14:15]
	v_cndmask_b32_e64 v55, v55, v54, s[14:15]
	v_cndmask_b32_e64 v84, v56, v57, s[14:15]
	v_cndmask_b32_e64 v57, v57, v56, s[14:15]
	v_cndmask_b32_e64 v85, v58, v59, s[14:15]
	v_cndmask_b32_e64 v59, v59, v58, s[14:15]
	v_cndmask_b32_e64 v86, v60, v61, s[14:15]
	v_cndmask_b32_e64 v61, v61, v60, s[14:15]
	v_cndmask_b32_e64 v87, v62, v63, s[14:15]
	v_cndmask_b32_e64 v63, v63, v62, s[14:15]
	v_cndmask_b32_e64 v88, v64, v65, s[14:15]
	v_cndmask_b32_e64 v65, v65, v64, s[14:15]
	v_cndmask_b32_e64 v89, v66, v67, s[14:15]
	v_cndmask_b32_e64 v67, v67, v66, s[14:15]
	v_cndmask_b32_e64 v90, v68, v69, s[14:15]
	v_cndmask_b32_e64 v69, v69, v68, s[14:15]
	v_cndmask_b32_e64 v91, v70, v71, s[14:15]
	v_cndmask_b32_e64 v71, v71, v70, s[14:15]
	v_cndmask_b32_e64 v92, v72, v73, s[14:15]
	v_cndmask_b32_e64 v73, v73, v72, s[14:15]
	v_cndmask_b32_e64 v93, v74, v75, s[14:15]
	v_cndmask_b32_e64 v75, v75, v74, s[14:15]
	v_cndmask_b32_e64 v94, v76, v77, s[14:15]
	v_cndmask_b32_e64 v77, v77, v76, s[14:15]
	v_cndmask_b32_e64 v95, v78, v79, s[14:15]
	v_cndmask_b32_e64 v79, v79, v78, s[14:15]
	v_add_f32_dpp v43, v43, v43 row_shr:2 row_mask:0xf bank_mask:0xf
	v_add_f32_dpp v48, v49, v80 quad_perm:[1,0,3,2] row_mask:0xf bank_mask:0xf
	v_add_f32_dpp v50, v51, v81 quad_perm:[1,0,3,2] row_mask:0xf bank_mask:0xf
	v_add_f32_dpp v52, v53, v82 quad_perm:[1,0,3,2] row_mask:0xf bank_mask:0xf
	v_add_f32_dpp v54, v55, v83 quad_perm:[1,0,3,2] row_mask:0xf bank_mask:0xf
	v_add_f32_dpp v56, v57, v84 quad_perm:[1,0,3,2] row_mask:0xf bank_mask:0xf
	v_add_f32_dpp v58, v59, v85 quad_perm:[1,0,3,2] row_mask:0xf bank_mask:0xf
	v_add_f32_dpp v60, v61, v86 quad_perm:[1,0,3,2] row_mask:0xf bank_mask:0xf
	v_add_f32_dpp v62, v63, v87 quad_perm:[1,0,3,2] row_mask:0xf bank_mask:0xf
	v_add_f32_dpp v64, v65, v88 quad_perm:[1,0,3,2] row_mask:0xf bank_mask:0xf
	v_add_f32_dpp v66, v67, v89 quad_perm:[1,0,3,2] row_mask:0xf bank_mask:0xf
	v_add_f32_dpp v68, v69, v90 quad_perm:[1,0,3,2] row_mask:0xf bank_mask:0xf
	v_add_f32_dpp v70, v71, v91 quad_perm:[1,0,3,2] row_mask:0xf bank_mask:0xf
	v_add_f32_dpp v72, v73, v92 quad_perm:[1,0,3,2] row_mask:0xf bank_mask:0xf
	v_add_f32_dpp v74, v75, v93 quad_perm:[1,0,3,2] row_mask:0xf bank_mask:0xf
	v_add_f32_dpp v76, v77, v94 quad_perm:[1,0,3,2] row_mask:0xf bank_mask:0xf
	v_add_f32_dpp v78, v79, v95 quad_perm:[1,0,3,2] row_mask:0xf bank_mask:0xf
	v_add_f32_dpp v43, v43, v43 row_shr:4 row_mask:0xf bank_mask:0xf
	v_cndmask_b32_e64 v80, v48, v50, s[24:25]
	v_cndmask_b32_e64 v50, v50, v48, s[24:25]
	v_cndmask_b32_e64 v81, v52, v54, s[24:25]
	v_cndmask_b32_e64 v54, v54, v52, s[24:25]
	v_cndmask_b32_e64 v82, v56, v58, s[24:25]
	v_cndmask_b32_e64 v58, v58, v56, s[24:25]
	v_cndmask_b32_e64 v83, v60, v62, s[24:25]
	v_cndmask_b32_e64 v62, v62, v60, s[24:25]
	v_cndmask_b32_e64 v84, v64, v66, s[24:25]
	v_cndmask_b32_e64 v66, v66, v64, s[24:25]
	v_cndmask_b32_e64 v85, v68, v70, s[24:25]
	v_cndmask_b32_e64 v70, v70, v68, s[24:25]
	v_cndmask_b32_e64 v86, v72, v74, s[24:25]
	v_cndmask_b32_e64 v74, v74, v72, s[24:25]
	v_cndmask_b32_e64 v87, v76, v78, s[24:25]
	v_cndmask_b32_e64 v78, v78, v76, s[24:25]
	v_add_f32_dpp v43, v43, v43 row_shr:8 row_mask:0xf bank_mask:0xf
	v_add_f32_dpp v48, v50, v80 quad_perm:[2,3,0,1] row_mask:0xf bank_mask:0xf
	v_add_f32_dpp v52, v54, v81 quad_perm:[2,3,0,1] row_mask:0xf bank_mask:0xf
	v_add_f32_dpp v56, v58, v82 quad_perm:[2,3,0,1] row_mask:0xf bank_mask:0xf
	v_add_f32_dpp v60, v62, v83 quad_perm:[2,3,0,1] row_mask:0xf bank_mask:0xf
	v_add_f32_dpp v64, v66, v84 quad_perm:[2,3,0,1] row_mask:0xf bank_mask:0xf
	v_add_f32_dpp v68, v70, v85 quad_perm:[2,3,0,1] row_mask:0xf bank_mask:0xf
	v_add_f32_dpp v72, v74, v86 quad_perm:[2,3,0,1] row_mask:0xf bank_mask:0xf
	v_add_f32_dpp v76, v78, v87 quad_perm:[2,3,0,1] row_mask:0xf bank_mask:0xf
	v_add_f32_dpp v48, v48, v48 row_shr:4 row_mask:0xf bank_mask:0xf
	v_add_f32_dpp v52, v52, v52 row_shr:4 row_mask:0xf bank_mask:0xf
	v_add_f32_dpp v56, v56, v56 row_shr:4 row_mask:0xf bank_mask:0xf
	v_add_f32_dpp v60, v60, v60 row_shr:4 row_mask:0xf bank_mask:0xf
	v_add_f32_dpp v64, v64, v64 row_shr:4 row_mask:0xf bank_mask:0xf
	v_add_f32_dpp v68, v68, v68 row_shr:4 row_mask:0xf bank_mask:0xf
	v_add_f32_dpp v72, v72, v72 row_shr:4 row_mask:0xf bank_mask:0xf
	v_add_f32_dpp v76, v76, v76 row_shr:4 row_mask:0xf bank_mask:0xf
	v_add_f32_dpp v48, v48, v48 row_shr:8 row_mask:0xf bank_mask:0xf
	v_add_f32_dpp v52, v52, v52 row_shr:8 row_mask:0xf bank_mask:0xf
	v_add_f32_dpp v56, v56, v56 row_shr:8 row_mask:0xf bank_mask:0xf
	v_add_f32_dpp v60, v60, v60 row_shr:8 row_mask:0xf bank_mask:0xf
	v_add_f32_dpp v64, v64, v64 row_shr:8 row_mask:0xf bank_mask:0xf
	v_add_f32_dpp v68, v68, v68 row_shr:8 row_mask:0xf bank_mask:0xf
	v_add_f32_dpp v72, v72, v72 row_shr:8 row_mask:0xf bank_mask:0xf
	v_add_f32_dpp v76, v76, v76 row_shr:8 row_mask:0xf bank_mask:0xf
	s_mov_b64 s[28:29], exec
	s_mov_b32 exec_lo, 0xf000f000
	s_mov_b32 exec_hi, 0xf000f000
	ds_write_b32 v47, v48
	ds_write_b32 v47, v52 offset:64
	ds_write_b32 v47, v56 offset:128
	ds_write_b32 v47, v60 offset:192
	ds_write_b32 v47, v64 offset:256
	ds_write_b32 v47, v68 offset:320
	ds_write_b32 v47, v72 offset:384
	ds_write_b32 v47, v76 offset:448
	s_mov_b64 exec, s[4:5]
	v_mov_b32_e32 v44, s37
	ds_write_b64 v44, v[42:43] offset:512
	s_mov_b64 exec, s[28:29]
	v_lshrrev_b32_e32 v42, 7, v0
	s_movk_i32 s4, 0x1080
	v_mov_b32_e32 v43, 0x23440
	s_waitcnt vmcnt(11)
	v_mad_u32_u24 v59, v42, s4, v43
	s_waitcnt lgkmcnt(0)
	s_barrier
	ds_read_b32 v46, v59 offset:512
	ds_read_b32 v47, v59 offset:1040
	ds_read_b32 v50, v59 offset:1568
	ds_read_b32 v51, v59 offset:2096
	ds_read_b64 v[42:43], v59 offset:1040
	ds_read_b64 v[44:45], v59 offset:512
	s_mov_b32 s4, 0xff800000
	s_waitcnt vmcnt(8)
	v_cvt_pk_bf16_f32 v30, v30, v31
	v_cvt_pk_bf16_f32 v31, v32, v33
	s_waitcnt lgkmcnt(4)
	v_max3_f32 v52, v46, s4, v47
	ds_read_b64 v[46:47], v59 offset:2096
	ds_read_b64 v[48:49], v59 offset:1568
	s_waitcnt lgkmcnt(4)
	v_max3_f32 v54, v52, v50, v51
	ds_read_b32 v55, v59 offset:2624
	ds_read_b32 v56, v59 offset:3152
	ds_read_b32 v58, v59 offset:3680
	ds_read_b32 v60, v59 offset:4208
	ds_read_b64 v[50:51], v59 offset:3152
	ds_read_b64 v[52:53], v59 offset:2624
	s_waitcnt lgkmcnt(4)
	v_max3_f32 v61, v54, v55, v56
	ds_read_b64 v[54:55], v59 offset:4208
	ds_read_b64 v[56:57], v59 offset:3680
	s_waitcnt lgkmcnt(4)
	v_max3_f32 v63, v61, v58, v60
	v_and_b32_e32 v60, 0x1fc, v130
	v_sub_f32_e32 v44, v44, v63
	v_sub_f32_e32 v42, v42, v63
	v_exp_f32_e32 v58, v44
	v_add_u32_e32 v44, v59, v60
	v_exp_f32_e32 v62, v42
	v_sub_f32_e32 v42, v48, v63
	v_exp_f32_e32 v64, v42
	v_add_u32_e32 v42, 0x400, v44
	ds_read2_b32 v[66:67], v42 offset0:8 offset1:140
	v_sub_f32_e32 v42, v46, v63
	ds_read2_b32 v[60:61], v44 offset1:132
	v_exp_f32_e32 v68, v42
	s_waitcnt lgkmcnt(4)
	v_sub_f32_e32 v42, v52, v63
	v_exp_f32_e32 v70, v42
	v_add_u32_e32 v42, 0x800, v44
	ds_read2_b32 v[72:73], v42 offset0:16 offset1:148
	v_sub_f32_e32 v42, v50, v63
	s_waitcnt vmcnt(7)
	v_exp_f32_e32 v74, v42
	s_waitcnt lgkmcnt(3)
	v_sub_f32_e32 v42, v56, v63
	v_exp_f32_e32 v76, v42
	v_add_u32_e32 v42, 0xc00, v44
	s_waitcnt vmcnt(6)
	ds_read2_b32 v[78:79], v42 offset0:24 offset1:156
	v_sub_f32_e32 v42, v54, v63
	s_waitcnt lgkmcnt(2)
	v_mov_b32_e32 v44, v60
	v_exp_f32_e32 v80, v42
	v_pk_fma_f32 v[44:45], v[44:45], v[58:59], 0 op_sel_hi:[1,0,0]
	v_mov_b32_e32 v42, v61
	v_pk_fma_f32 v[42:43], v[42:43], v[62:63], v[44:45] op_sel_hi:[1,0,1]
	v_mov_b32_e32 v48, v66
	v_pk_fma_f32 v[42:43], v[48:49], v[64:65], v[42:43] op_sel_hi:[1,0,1]
	v_mov_b32_e32 v46, v67
	v_pk_fma_f32 v[42:43], v[46:47], v[68:69], v[42:43] op_sel_hi:[1,0,1]
	s_waitcnt lgkmcnt(1)
	v_mov_b32_e32 v52, v72
	v_pk_fma_f32 v[42:43], v[52:53], v[70:71], v[42:43] op_sel_hi:[1,0,1]
	v_mov_b32_e32 v50, v73
	v_pk_fma_f32 v[42:43], v[50:51], v[74:75], v[42:43] op_sel_hi:[1,0,1]
	s_waitcnt lgkmcnt(0)
	v_mov_b32_e32 v56, v78
	v_pk_fma_f32 v[42:43], v[56:57], v[76:77], v[42:43] op_sel_hi:[1,0,1]
	v_mov_b32_e32 v54, v79
	v_pk_fma_f32 v[42:43], v[54:55], v[80:81], v[42:43] op_sel_hi:[1,0,1]
	v_cvt_pk_bf16_f32 v32, v26, v27
	v_div_scale_f32 v44, s[4:5], v43, v43, v42
	v_rcp_f32_e32 v45, v44
	s_movk_i32 s4, 0x600
	v_cvt_pk_bf16_f32 v33, v28, v29
	v_cvt_pk_bf16_f32 v22, v22, v23
	v_fma_f32 v46, -v44, v45, 1.0
	v_fmac_f32_e32 v45, v46, v45
	v_div_scale_f32 v46, vcc, v42, v43, v42
	v_mul_f32_e32 v47, v46, v45
	v_fma_f32 v48, -v44, v47, v46
	v_fmac_f32_e32 v47, v48, v45
	v_fma_f32 v44, -v44, v47, v46
	v_div_fmas_f32 v44, v44, v45, v47
	v_div_fixup_f32 v42, v44, v43, v42
	v_fma_f32 v42, v42, -2.0, 1.0
	v_add_u32_e32 v43, 0x22400, v130
	ds_write_b32 v43, v42
	v_lshlrev_b32_e32 v42, 9, v0
	v_and_or_b32 v42, v42, s4, v132
	v_add_u32_e32 v50, 0x22400, v42
	s_waitcnt lgkmcnt(0)
	s_barrier
	ds_read_b128 v[42:45], v50
	ds_read_b128 v[46:49], v50 offset:16
	v_cvt_pk_bf16_f32 v23, v24, v25
	v_cvt_pk_bf16_f32 v24, v18, v19
	v_cvt_pk_bf16_f32 v25, v20, v21
	s_waitcnt lgkmcnt(1)
	v_cvt_pk_bf16_f32 v26, v42, v43
	v_cvt_pk_bf16_f32 v27, v44, v45
	s_waitcnt lgkmcnt(0)
	v_cvt_pk_bf16_f32 v28, v46, v47
	v_cvt_pk_bf16_f32 v29, v48, v49
	ds_read_b128 v[42:45], v50 offset:144
	s_waitcnt vmcnt(4)
	v_cvt_pk_bf16_f32 v14, v14, v15
	v_mfma_f32_16x16x32_bf16 v[26:29], v[30:33], v[26:29], 0
	ds_read_b128 v[30:33], v50 offset:128
	v_cvt_pk_bf16_f32 v15, v16, v17
	s_waitcnt lgkmcnt(1)
	v_cvt_pk_bf16_f32 v20, v42, v43
	v_cvt_pk_bf16_f32 v21, v44, v45
	v_cvt_pk_bf16_f32 v16, v10, v11
	s_waitcnt lgkmcnt(0)
	v_cvt_pk_bf16_f32 v18, v30, v31
	v_cvt_pk_bf16_f32 v19, v32, v33
	v_cvt_pk_bf16_f32 v17, v12, v13
	s_waitcnt vmcnt(2)
	v_cvt_pk_bf16_f32 v6, v6, v7
	v_mfma_f32_16x16x32_bf16 v[18:21], v[22:25], v[18:21], v[26:29]
	ds_read_b128 v[22:25], v50 offset:256
	v_cvt_pk_bf16_f32 v7, v8, v9
	v_cvt_pk_bf16_f32 v8, v2, v3
	ds_read_b128 v[26:29], v50 offset:272
	v_cvt_pk_bf16_f32 v9, v4, v5
	s_waitcnt lgkmcnt(1)
	v_cvt_pk_bf16_f32 v10, v22, v23
	v_cvt_pk_bf16_f32 v11, v24, v25
	s_mov_b32 s4, 0x3f200000
	s_waitcnt lgkmcnt(0)
	v_cvt_pk_bf16_f32 v12, v26, v27
	v_cvt_pk_bf16_f32 v13, v28, v29
	s_nop 1
	v_mfma_f32_16x16x32_bf16 v[10:13], v[14:17], v[10:13], v[18:21]
	ds_read_b128 v[14:17], v50 offset:384
	s_nop 1
	ds_read_b128 v[18:21], v50 offset:400
	s_waitcnt lgkmcnt(1)
	v_cvt_pk_bf16_f32 v2, v14, v15
	v_cvt_pk_bf16_f32 v3, v16, v17
	s_waitcnt lgkmcnt(0)
	v_cvt_pk_bf16_f32 v4, v18, v19
	v_cvt_pk_bf16_f32 v5, v20, v21
	s_nop 1
	v_mfma_f32_16x16x32_bf16 v[2:5], v[6:9], v[2:5], v[10:13]
	s_waitcnt vmcnt(1)
	s_nop 6
	v_add_f32_e32 v2, v2, v38
	v_add_f32_e32 v3, v3, v39
	v_add_f32_e32 v4, v4, v40
	v_add_f32_e32 v5, v5, v41
	v_mul_f32_e32 v6, 0x4038aa3b, v2
	v_mul_f32_e32 v7, 0x4038aa3b, v3
	v_mul_f32_e32 v8, 0x4038aa3b, v4
	v_mul_f32_e32 v9, 0x4038aa3b, v5
	v_exp_f32_e32 v6, v6
	v_exp_f32_e32 v7, v7
	v_exp_f32_e32 v8, v8
	v_exp_f32_e32 v9, v9
	v_add_f32_e32 v6, 1.0, v6
	v_add_f32_e32 v7, 1.0, v7
	v_add_f32_e32 v8, 1.0, v8
	v_add_f32_e32 v9, 1.0, v9
	v_rcp_f32_e32 v6, v6
	v_rcp_f32_e32 v7, v7
	v_rcp_f32_e32 v8, v8
	v_rcp_f32_e32 v9, v9
	v_fma_f32 v2, v6, -2.0, 1.0
	v_fma_f32 v3, v7, -2.0, 1.0
	v_fma_f32 v4, v8, -2.0, 1.0
	v_fma_f32 v5, v9, -2.0, 1.0
	v_cmp_gt_u32_e32 vcc, 4, v202
	s_and_saveexec_b64 s[4:5], vcc
	s_andn2_b32 s3, s3, 63
	v_lshl_or_b32 v6, v202, 9, v203
	v_add_u32_e32 v6, s3, v6
	v_add_u32_e32 v6, 0x22c00, v6
	ds_write_b128 v6, v[2:5]
	s_or_b64 exec, exec, s[4:5]
	s_waitcnt vmcnt(0)
	v_fma_f32 v2, v2, v34, 0
	v_fmac_f32_e32 v2, v3, v35
	v_fmac_f32_e32 v2, v4, v36
	v_fmac_f32_e32 v2, v5, v37
	ds_bpermute_b32 v3, v201, v2
	v_cmp_gt_u32_e32 vcc, 4, v131
	s_waitcnt lgkmcnt(0)
	v_add_f32_e32 v2, v2, v3
	ds_bpermute_b32 v3, v200, v2
	s_and_saveexec_b64 s[4:5], vcc
	s_cbranch_execz .LBB0_78
	v_add_u32_e32 v1, s30, v1
	v_add_u32_e32 v1, 0x23440, v1
	s_waitcnt lgkmcnt(0)
	v_add_f32_e32 v2, v2, v3
	ds_write_b32 v1, v2
